# SB attention P.V block: V transposed reads first into their own registers, row-total adds and bf16 packs dealt into the LDS latency and the P.V MFMA gaps (was a VALU-only block in front of 8 bare MFMA
# speedup vs baseline: 1.0068x; 1.0054x over previous
; #define LAS __attribute__((address_space(3)))
; __device__ __forceinline__ float ex2(float x) { return __builtin_amdgcn_exp2f(x); }
; __device__ __forceinline__ f32x16 mfma32(bf16x8 a, bf16x8 b, f32x16 c) { return __builtin_amdgcn_mfma_f32_32x32x16_bf16(a, b, c, 0, 0, 0); }
; __device__ __forceinline__ s16x4 vtr(const LAS unsigned char* p) { return __builtin_bit_cast(s16x4, __builtin_amdgcn_ds_read_tr16_b64_v4i16((LAS v4i16_t*)p)); }
; __device__ __forceinline__ float swapsum(float m) { auto rr = __builtin_amdgcn_permlane32_swap(__float_as_uint(m), __float_as_uint(m), false, false); return __uint_as_float(rr[0]) + __uint_as_float(rr[1]); }
; __device__ __forceinline__ u32x4 packp(const f32x16& p, int b) { u32x4 w; w.x = cvt_pk_bf16(p[b], p[b + 1]); w.y = cvt_pk_bf16(p[b + 2], p[b + 3]); w.z = cvt_pk_bf16(p[b + 4], p[b + 5]); w.w = cvt_pk_bf16(p[b + 6], p[b + 7]); return w; }
; __device__ __forceinline__ void pv(f32x16 (&o)[2], const LAS unsigned char* vp, u32x4 pw0, u32x4 pw1, u32x4 pw2, u32x4 pw3) {
; #pragma unroll
;     for (int d0 = 0; d0 < 2; ++d0) {
;         s16x4 lo[4], hi4[4];
; #pragma unroll
;         for (int ks = 0; ks < 4; ++ks) { lo[ks] = vtr(vp + d0 * 4096 + ks * 1024); hi4[ks] = vtr(vp + d0 * 4096 + ks * 1024 + 512); }
;     ...
;         o[d0] = mfma32(__builtin_bit_cast(bf16x8, pw0), ATT_PK(0), o[d0]);
;         o[d0] = mfma32(__builtin_bit_cast(bf16x8, pw1), ATT_PK(1), o[d0]);
;         o[d0] = mfma32(__builtin_bit_cast(bf16x8, pw2), ATT_PK(2), o[d0]);
;         o[d0] = mfma32(__builtin_bit_cast(bf16x8, pw3), ATT_PK(3), o[d0]);
;     ...
;     }
; }
; __device__ __forceinline__ void sb_unit(int b, int h, int qb, const bf16_t* __restrict__ PROJ, bf16_t* OCAT, float* SSQO, ldsp shm, volatile LAS unsigned* FL) {
;     ...
;             for (int r = 0; r < 16; ++r) { z0[r] = ex2(z0[r] + x0[r]); z1[r] = ex2(z1[r] + x1[r]); }
;             if (diag) {
; #pragma unroll
;                 for (int r = 0; r < 16; ++r) { const int kk = kb0 + (r & 3) + 8 * (r >> 2); if (kk >= qabs) z0[r] = 0.f; if (kk + 32 >= qabs) z1[r] = 0.f; } }
;             pv(o, vp0 + (step & 3) * VS, packp(z0, 0), packp(z0, 8), packp(z1, 0), packp(z1, 8));
;             Lc += swapsum(tot);
;             wfin = __all(Lc <= SB_DONE) != 0;
.LBB0_1060:
	v_add_u32_e32 v99, s8, v162
	ds_read_b64_tr_b16 v[100:101], v99 offset:32768
	ds_read_b64_tr_b16 v[102:103], v99 offset:33280
	ds_read_b64_tr_b16 v[104:105], v99 offset:33792
	ds_read_b64_tr_b16 v[106:107], v99 offset:34304
	ds_read_b64_tr_b16 v[108:109], v99 offset:34816
	ds_read_b64_tr_b16 v[110:111], v99 offset:35328
	ds_read_b64_tr_b16 v[200:201], v99 offset:35840
	ds_read_b64_tr_b16 v[202:203], v99 offset:36352
	v_cvt_pk_bf16_f32 v114, v84, v83
	v_cvt_pk_bf16_f32 v115, v88, v87
	v_cvt_pk_bf16_f32 v116, v92, v91
	v_cvt_pk_bf16_f32 v117, v96, v95
	v_add_f32_e32 v2, v2, v52
	v_add_f32_e32 v1, v1, v53
	v_add_f32_e32 v52, v54, v56
	v_add_f32_e32 v1, v1, v2
	v_add_f32_e32 v53, v55, v57
	v_add_f32_e32 v1, v52, v1
	v_add_f32_e32 v54, v58, v60
	v_add_f32_e32 v1, v53, v1
	v_add_f32_e32 v55, v59, v61
	v_add_f32_e32 v1, v54, v1
	v_add_f32_e32 v56, v62, v64
	v_add_f32_e32 v1, v55, v1
	s_mov_b32 s0, 0x43160000
	s_movk_i32 s80, 0xff
	s_mov_b32 s81, 0x41000000
	s_mov_b64 s[82:83], 0x800
	s_mov_b64 s[84:85], 0xc00
	s_mov_b64 s[86:87], 0x70000
	s_mov_b64 s[88:89], 0x70080
	s_waitcnt lgkmcnt(0)
	v_mfma_f32_32x32x16_bf16 v[20:35], v[114:117], v[100:103], v[20:35]
	v_cvt_pk_bf16_f32 v118, v86, v85
	v_cvt_pk_bf16_f32 v119, v90, v89
	v_cvt_pk_bf16_f32 v120, v94, v93
	v_cvt_pk_bf16_f32 v121, v98, v97
	v_add_f32_e32 v57, v63, v65
	v_add_f32_e32 v1, v56, v1
	v_mfma_f32_32x32x16_bf16 v[20:35], v[118:121], v[104:107], v[20:35]
	v_cvt_pk_bf16_f32 v122, v38, v37
	v_cvt_pk_bf16_f32 v123, v42, v41
	v_cvt_pk_bf16_f32 v124, v46, v45
	v_cvt_pk_bf16_f32 v125, v50, v49
	v_add_f32_e32 v58, v66, v68
	v_add_f32_e32 v1, v57, v1
	v_mfma_f32_32x32x16_bf16 v[20:35], v[122:125], v[108:111], v[20:35]
	v_cvt_pk_bf16_f32 v126, v40, v39
	v_cvt_pk_bf16_f32 v127, v44, v43
	v_cvt_pk_bf16_f32 v128, v48, v47
	v_cvt_pk_bf16_f32 v129, v82, v51
	v_add_f32_e32 v59, v67, v69
	v_add_f32_e32 v1, v58, v1
	v_mfma_f32_32x32x16_bf16 v[20:35], v[126:129], v[200:203], v[20:35]
	ds_read_b64_tr_b16 v[100:101], v99 offset:36864
	ds_read_b64_tr_b16 v[102:103], v99 offset:37376
	ds_read_b64_tr_b16 v[104:105], v99 offset:37888
	ds_read_b64_tr_b16 v[106:107], v99 offset:38400
	ds_read_b64_tr_b16 v[108:109], v99 offset:38912
	ds_read_b64_tr_b16 v[110:111], v99 offset:39424
	ds_read_b64_tr_b16 v[200:201], v99 offset:39936
	ds_read_b64_tr_b16 v[202:203], v99 offset:40448
	v_add_f32_e32 v60, v70, v72
	v_add_f32_e32 v1, v59, v1
	v_add_f32_e32 v61, v71, v73
	v_add_f32_e32 v1, v60, v1
	v_add_f32_e32 v62, v74, v76
	v_add_f32_e32 v1, v61, v1
	s_waitcnt lgkmcnt(0)
	v_mfma_f32_32x32x16_bf16 v[4:19], v[114:117], v[100:103], v[4:19]
	v_add_f32_e32 v63, v75, v77
	v_add_f32_e32 v1, v62, v1
	v_add_f32_e32 v64, v78, v80
	v_add_f32_e32 v1, v63, v1
	v_add_f32_e32 v65, v79, v81
	v_add_f32_e32 v1, v64, v1
	v_mfma_f32_32x32x16_bf16 v[4:19], v[118:121], v[104:107], v[4:19]
	v_add_f32_e32 v1, v65, v1
	v_mov_b32_e32 v2, v1
	s_nop 1
	v_permlane32_swap_b32_e32 v1, v2
	v_add_f32_e32 v1, v1, v2
	v_add_f32_e32 v36, v36, v1
	v_cmp_le_f32_e32 vcc, s0, v36
	v_mfma_f32_32x32x16_bf16 v[4:19], v[122:125], v[108:111], v[4:19]
	v_mfma_f32_32x32x16_bf16 v[4:19], v[126:129], v[200:203], v[4:19]
	s_cmp_eq_u64 vcc, exec
	s_cselect_b64 s[0:1], -1, 0
